# scan R1: second-tile LDS reads hoisted in the squaring stages; S0 cross-wave prefix reads issued together
# baseline (speedup 1.0000x reference)
.LBB0_1832:
	v_add_u32_e32 v26, v109, v110
	v_add_u32_e32 v58, v111, v142
	s_waitcnt lgkmcnt(0)
	s_barrier
	ds_read_b128 v[38:41], v26
	ds_read_b128 v[42:45], v26 offset:18432
	ds_read_b128 v[46:49], v26 offset:64
	ds_read_b128 v[50:53], v26 offset:18496
	ds_read_b128 v[26:29], v58 offset:27648
	ds_read_b128 v[30:33], v58 offset:46080
	s_waitcnt lgkmcnt(1)
	v_mfma_f32_16x16x32_bf16 v[34:37], v[26:29], v[38:41], 0
	ds_read_b128 v[60:63], v58 offset:27712
	ds_read_b128 v[64:67], v58 offset:46144
	s_or_b64 vcc, s[52:53], s[28:29]
	v_add_u32_e32 v82, v111, v145
	v_mfma_f32_16x16x32_bf16 v[26:29], v[26:29], v[42:45], 0
	v_add_u32_e32 v72, v113, v146
	v_add_u32_e32 v73, v122, v146
	v_add_u32_e32 v74, v112, v110
	s_waitcnt lgkmcnt(2)
	v_mfma_f32_16x16x32_bf16 v[54:57], v[30:33], v[38:41], 0
	v_add_u32_e32 v78, v123, v145
	v_add_u32_e32 v75, v121, v110
	v_add_u32_e32 v76, v130, v142
	v_mfma_f32_16x16x32_bf16 v[30:33], v[30:33], v[42:45], 0
	s_ashr_i32 s87, s86, 31
	s_lshl_b64 s[76:77], s[86:87], 12
	v_lshl_add_u64 v[106:107], v[90:91], 0, s[76:77]
	s_waitcnt lgkmcnt(1)
	v_mfma_f32_16x16x32_bf16 v[26:29], v[60:63], v[50:53], v[26:29]
	v_readlane_b32 s76, v252, 13
	v_readlane_b32 s77, v252, 14
	s_mov_b32 s86, s33
	v_mfma_f32_16x16x32_bf16 v[34:37], v[60:63], v[46:49], v[34:37]
	v_mov_b32_e32 v60, s83
	v_mov_b32_e32 v62, s83
	s_nop 1
	v_cndmask_b32_e64 v60, v26, v60, s[30:31]
	s_waitcnt lgkmcnt(0)
	v_mfma_f32_16x16x32_bf16 v[54:57], v[64:67], v[46:49], v[54:57]
	v_cndmask_b32_e64 v60, v60, v26, s[28:29]
	v_cndmask_b32_e64 v61, 0, v27, s[28:29]
	v_cndmask_b32_e64 v27, 0, v35, s[52:53]
	v_mfma_f32_16x16x32_bf16 v[30:33], v[64:67], v[50:53], v[30:33]
	v_cndmask_b32_e32 v26, 0, v34, vcc
	s_nop 2
	v_cndmask_b32_e32 v64, 0, v54, vcc
	v_cndmask_b32_e64 v54, 0, v36, s[50:51]
	v_cndmask_b32_e64 v63, v28, 0, s[34:35]
	v_cndmask_b32_e64 v56, 0, v56, s[50:51]
	v_cndmask_b32_e64 v59, v30, v62, s[30:31]
	v_cndmask_b32_e64 v62, v32, 0, s[34:35]
	v_cndmask_b32_e64 v32, 0, v57, s[36:37]
	v_cndmask_b32_e64 v57, 0, v55, s[52:53]
	v_cndmask_b32_e64 v55, 0, v37, s[36:37]
	v_cndmask_b32_e64 v59, v59, v30, s[28:29]
	v_cndmask_b32_e64 v34, v29, 0, s[38:39]
	v_cvt_pk_bf16_f32 v28, v26, v27
	v_cvt_pk_bf16_f32 v29, v54, v55
	v_add_u32_e32 v36, v113, v143
	v_add_u32_e32 v30, v114, v144
	ds_write_b64 v36, v[28:29]
	ds_write_b16 v30, v28
	ds_write_b16_d16_hi v30, v28 offset:144
	ds_write_b16 v30, v29 offset:288
	ds_write_b16_d16_hi v30, v29 offset:432
	v_cvt_pk_bf16_f32 v28, v64, v57
	v_cvt_pk_bf16_f32 v29, v56, v32
	v_add_u32_e32 v32, v116, v143
	v_cndmask_b32_e64 v31, 0, v31, s[28:29]
	v_cndmask_b32_e64 v33, v33, 0, s[38:39]
	ds_write_b64 v32, v[28:29]
	v_cvt_pk_bf16_f32 v28, v60, v61
	v_cvt_pk_bf16_f32 v29, v63, v34
	v_add_u32_e32 v34, v118, v143
	ds_write_b64 v34, v[28:29]
	v_cvt_pk_bf16_f32 v28, v59, v31
	v_cvt_pk_bf16_f32 v29, v62, v33
	v_add_u32_e32 v31, v120, v143
	ds_write_b64 v31, v[28:29]
	v_pk_add_f32 v[26:27], v[94:95], v[26:27]
	v_pk_add_f32 v[28:29], v[96:97], v[54:55]
	v_cvt_pk_bf16_f32 v54, v26, v27
	v_cvt_pk_bf16_f32 v55, v28, v29
	v_add_u32_e32 v34, v122, v143
	ds_write_b64 v34, v[54:55]
	ds_read_b128 v[54:57], v82 offset:27648
	ds_read_b128 v[60:63], v82 offset:46080
	s_waitcnt lgkmcnt(1)
	v_mfma_f32_16x16x32_bf16 v[64:67], v[54:57], v[38:41], 0
	s_or_b64 vcc, s[56:57], s[40:41]
	v_add_u32_e32 v59, v123, v142
	s_waitcnt lgkmcnt(0)
	v_mfma_f32_16x16x32_bf16 v[38:41], v[60:63], v[38:41], 0
	v_mfma_f32_16x16x32_bf16 v[54:57], v[54:57], v[42:45], 0
	v_mfma_f32_16x16x32_bf16 v[42:45], v[60:63], v[42:45], 0
	ds_read_b128 v[60:63], v82 offset:27712
	ds_read_b128 v[68:71], v82 offset:46144
	s_waitcnt lgkmcnt(1)
	v_mfma_f32_16x16x32_bf16 v[64:67], v[60:63], v[46:49], v[64:67]
	s_waitcnt lgkmcnt(0)
	v_mfma_f32_16x16x32_bf16 v[38:41], v[68:71], v[46:49], v[38:41]
	v_mfma_f32_16x16x32_bf16 v[46:49], v[60:63], v[50:53], v[54:57]
	v_mfma_f32_16x16x32_bf16 v[42:45], v[68:71], v[50:53], v[42:45]
	v_mov_b32_e32 v50, s83
	v_mov_b32_e32 v52, s83
	s_nop 4
	v_cndmask_b32_e64 v33, v46, v50, s[42:43]
	v_cndmask_b32_e64 v46, v33, v46, s[40:41]
	v_cndmask_b32_e64 v33, 0, v41, s[46:47]
	v_cndmask_b32_e64 v31, v42, v52, s[42:43]
	v_cndmask_b32_e64 v50, 0, v40, s[54:55]
	v_cndmask_b32_e64 v51, 0, v39, s[56:57]
	v_cndmask_b32_e32 v52, 0, v38, vcc
	v_cndmask_b32_e64 v41, 0, v67, s[46:47]
	v_cndmask_b32_e64 v40, 0, v66, s[54:55]
	v_cndmask_b32_e64 v39, 0, v65, s[56:57]
	v_cndmask_b32_e32 v38, 0, v64, vcc
	v_cndmask_b32_e64 v35, v31, v42, s[40:41]
	v_cndmask_b32_e64 v37, 0, v43, s[40:41]
	v_cvt_pk_bf16_f32 v42, v38, v39
	v_cvt_pk_bf16_f32 v43, v40, v41
	v_add_u32_e32 v31, v114, v147
	v_cndmask_b32_e64 v47, 0, v47, s[40:41]
	v_cndmask_b32_e64 v48, v48, 0, s[44:45]
	v_cndmask_b32_e64 v49, v49, 0, s[48:49]
	ds_write_b64 v72, v[42:43]
	ds_write_b16 v31, v42
	ds_write_b16_d16_hi v31, v42 offset:144
	ds_write_b16 v31, v43 offset:288
	ds_write_b16_d16_hi v31, v43 offset:432
	v_cvt_pk_bf16_f32 v42, v52, v51
	v_cvt_pk_bf16_f32 v43, v50, v33
	v_add_u32_e32 v33, v116, v146
	v_cndmask_b32_e64 v44, v44, 0, s[44:45]
	v_cndmask_b32_e64 v45, v45, 0, s[48:49]
	ds_write_b64 v33, v[42:43]
	v_cvt_pk_bf16_f32 v42, v46, v47
	v_cvt_pk_bf16_f32 v43, v48, v49
	v_add_u32_e32 v46, v118, v146
	ds_write_b64 v46, v[42:43]
	v_cvt_pk_bf16_f32 v42, v35, v37
	v_cvt_pk_bf16_f32 v43, v44, v45
	v_add_u32_e32 v35, v120, v146
	v_pk_add_f32 v[38:39], v[100:101], v[38:39]
	v_pk_add_f32 v[40:41], v[102:103], v[40:41]
	ds_write_b64 v35, v[42:43]
	v_cvt_pk_bf16_f32 v42, v38, v39
	v_cvt_pk_bf16_f32 v43, v40, v41
	v_add_u32_e32 v35, v115, v110
	ds_write_b64 v73, v[42:43]
	s_waitcnt lgkmcnt(0)
	s_barrier
	ds_read_b128 v[42:45], v35
	ds_read_b128 v[46:49], v74
	ds_read_b128 v[50:53], v35 offset:64
	ds_read_b128 v[54:57], v74 offset:64
	ds_read_b128 v[60:63], v58 offset:64512
	ds_read_b128 v[64:67], v59
	ds_read_b128 v[68:71], v58 offset:64576
	s_waitcnt lgkmcnt(2)
	v_mfma_f32_16x16x32_bf16 v[60:63], v[60:63], v[42:45], 0
	s_andn2_b64 vcc, exec, s[70:71]
	s_waitcnt lgkmcnt(0)
	v_mfma_f32_16x16x32_bf16 v[60:63], v[68:71], v[50:53], v[60:63]
	ds_read_b128 v[68:71], v59 offset:64
	v_mfma_f32_16x16x32_bf16 v[64:67], v[64:67], v[46:49], 0
	s_nop 5
	v_cvt_pk_bf16_f32 v37, v60, v61
	v_cvt_pk_bf16_f32 v60, v62, v63
	v_add_u32_e32 v61, v124, v144
	s_waitcnt lgkmcnt(0)
	v_mfma_f32_16x16x32_bf16 v[64:67], v[68:71], v[54:57], v[64:67]
	ds_write_b16 v61, v37
	ds_write_b16_d16_hi v61, v37 offset:144
	ds_write_b16 v61, v60 offset:288
	ds_write_b16_d16_hi v61, v60 offset:432
	v_add_u32_e32 v68, v126, v143
	v_add_u32_e32 v69, v127, v144
	s_nop 1
	v_cvt_pk_bf16_f32 v60, v64, v65
	v_cvt_pk_bf16_f32 v61, v66, v67
	ds_write_b64 v68, v[60:61] offset:27648
	ds_write_b16 v69, v60 offset:46080
	ds_write_b16_d16_hi v69, v60 offset:46224
	ds_write_b16 v69, v61 offset:46368
	ds_write_b16_d16_hi v69, v61 offset:46512
	ds_read_b128 v[60:63], v82 offset:64512
	s_waitcnt lgkmcnt(0)
	v_mfma_f32_16x16x32_bf16 v[42:45], v[60:63], v[42:45], 0
	ds_read_b128 v[60:63], v78
	v_add_u32_e32 v70, v126, v146
	v_add_u32_e32 v71, v127, v147
	s_waitcnt lgkmcnt(0)
	v_mfma_f32_16x16x32_bf16 v[46:49], v[60:63], v[46:49], 0
	ds_read_b128 v[60:63], v82 offset:64576
	s_waitcnt lgkmcnt(0)
	v_mfma_f32_16x16x32_bf16 v[42:45], v[60:63], v[50:53], v[42:45]
	ds_read_b128 v[50:53], v78 offset:64
	s_nop 6
	v_cvt_pk_bf16_f32 v37, v42, v43
	s_waitcnt lgkmcnt(0)
	v_mfma_f32_16x16x32_bf16 v[46:49], v[50:53], v[54:57], v[46:49]
	v_cvt_pk_bf16_f32 v42, v44, v45
	v_add_u32_e32 v43, v124, v147
	ds_write_b16 v43, v37
	ds_write_b16_d16_hi v43, v37 offset:144
	ds_write_b16 v43, v42 offset:288
	ds_write_b16_d16_hi v43, v42 offset:432
	s_nop 1
	v_cvt_pk_bf16_f32 v42, v46, v47
	v_cvt_pk_bf16_f32 v43, v48, v49
	v_add_u32_e32 v37, v125, v110
	ds_write_b64 v70, v[42:43] offset:27648
	ds_write_b16 v71, v42 offset:46080
	ds_write_b16_d16_hi v71, v42 offset:46224
	ds_write_b16 v71, v43 offset:46368
	ds_write_b16_d16_hi v71, v43 offset:46512
	s_waitcnt lgkmcnt(0)
	s_barrier
	ds_read_b128 v[42:45], v75
	ds_read_b128 v[46:49], v37 offset:27648
	ds_read_b128 v[50:53], v75 offset:64
	ds_read_b128 v[54:57], v37 offset:27712
	ds_read_b128 v[60:63], v58 offset:46080
	ds_read_b128 v[64:67], v58 offset:46144
	ds_read_b128 v[154:157], v82 offset:46080
	ds_read_b128 v[158:161], v82 offset:46144
	s_waitcnt lgkmcnt(3)
	v_mfma_f32_16x16x32_bf16 v[26:29], v[60:63], v[42:45], v[26:29]
	v_mfma_f32_16x16x32_bf16 v[60:63], v[60:63], v[46:49], 0
	s_waitcnt lgkmcnt(2)
	v_mfma_f32_16x16x32_bf16 v[26:29], v[64:67], v[50:53], v[26:29]
	v_mfma_f32_16x16x32_bf16 v[60:63], v[64:67], v[54:57], v[60:63]
	s_nop 6
	v_cvt_pk_bf16_f32 v64, v26, v27
	v_cvt_pk_bf16_f32 v65, v28, v29
	v_cvt_pk_bf16_f32 v60, v60, v61
	v_cvt_pk_bf16_f32 v61, v62, v63
	ds_write_b64 v32, v[64:65]
	ds_write_b64 v36, v[60:61]
	ds_write_b16 v30, v60
	ds_write_b16_d16_hi v30, v60 offset:144
	ds_write_b16 v30, v61 offset:288
	ds_write_b16_d16_hi v30, v61 offset:432
	s_waitcnt lgkmcnt(6)
	v_mfma_f32_16x16x32_bf16 v[38:41], v[154:157], v[42:45], v[38:41]
	v_mfma_f32_16x16x32_bf16 v[42:45], v[154:157], v[46:49], 0
	v_mfma_f32_16x16x32_bf16 v[38:41], v[158:161], v[50:53], v[38:41]
	v_mfma_f32_16x16x32_bf16 v[42:45], v[158:161], v[54:57], v[42:45]
	s_nop 6
	v_cvt_pk_bf16_f32 v46, v38, v39
	v_cvt_pk_bf16_f32 v47, v40, v41
	ds_write_b64 v33, v[46:47]
	v_cvt_pk_bf16_f32 v42, v42, v43
	v_cvt_pk_bf16_f32 v43, v44, v45
	ds_write_b64 v72, v[42:43]
	ds_write_b16 v31, v42
	ds_write_b16_d16_hi v31, v42 offset:144
	ds_write_b16 v31, v43 offset:288
	ds_write_b16_d16_hi v31, v43 offset:432
	s_waitcnt lgkmcnt(0)
	s_barrier
	ds_read_b128 v[42:45], v35
	ds_read_b128 v[46:49], v74
	ds_read_b128 v[50:53], v35 offset:64
	ds_read_b128 v[54:57], v74 offset:64
	ds_read_b128 v[60:63], v59
	ds_read_b128 v[64:67], v59 offset:64
	ds_read_b128 v[154:157], v78
	ds_read_b128 v[158:161], v78 offset:64
	s_waitcnt lgkmcnt(3)
	v_mfma_f32_16x16x32_bf16 v[26:29], v[60:63], v[42:45], v[26:29]
	v_mfma_f32_16x16x32_bf16 v[60:63], v[60:63], v[46:49], 0
	s_waitcnt lgkmcnt(2)
	v_mfma_f32_16x16x32_bf16 v[26:29], v[64:67], v[50:53], v[26:29]
	v_mfma_f32_16x16x32_bf16 v[60:63], v[64:67], v[54:57], v[60:63]
	s_nop 6
	v_cvt_pk_bf16_f32 v64, v26, v27
	v_cvt_pk_bf16_f32 v65, v28, v29
	v_cvt_pk_bf16_f32 v60, v60, v61
	v_cvt_pk_bf16_f32 v61, v62, v63
	ds_write_b64 v34, v[64:65]
	ds_write_b64 v68, v[60:61] offset:27648
	ds_write_b16 v69, v60 offset:46080
	ds_write_b16_d16_hi v69, v60 offset:46224
	ds_write_b16 v69, v61 offset:46368
	ds_write_b16_d16_hi v69, v61 offset:46512
	s_waitcnt lgkmcnt(6)
	v_mfma_f32_16x16x32_bf16 v[38:41], v[154:157], v[42:45], v[38:41]
	v_mfma_f32_16x16x32_bf16 v[42:45], v[154:157], v[46:49], 0
	v_mfma_f32_16x16x32_bf16 v[38:41], v[158:161], v[50:53], v[38:41]
	v_mfma_f32_16x16x32_bf16 v[42:45], v[158:161], v[54:57], v[42:45]
	s_nop 6
	v_cvt_pk_bf16_f32 v46, v38, v39
	v_cvt_pk_bf16_f32 v47, v40, v41
	ds_write_b64 v73, v[46:47]
	v_cvt_pk_bf16_f32 v42, v42, v43
	v_cvt_pk_bf16_f32 v43, v44, v45
	ds_write_b64 v70, v[42:43] offset:27648
	ds_write_b16 v71, v42 offset:46080
	ds_write_b16_d16_hi v71, v42 offset:46224
	ds_write_b16 v71, v43 offset:46368
	ds_write_b16_d16_hi v71, v43 offset:46512
	s_waitcnt lgkmcnt(0)
	s_barrier
	ds_read_b128 v[42:45], v75
	ds_read_b128 v[46:49], v37 offset:27648
	ds_read_b128 v[50:53], v75 offset:64
	ds_read_b128 v[54:57], v37 offset:27712
	ds_read_b128 v[60:63], v58 offset:46080
	ds_read_b128 v[64:67], v58 offset:46144
	ds_read_b128 v[154:157], v82 offset:46080
	ds_read_b128 v[158:161], v82 offset:46144
	s_waitcnt lgkmcnt(3)
	v_mfma_f32_16x16x32_bf16 v[26:29], v[60:63], v[42:45], v[26:29]
	v_mfma_f32_16x16x32_bf16 v[60:63], v[60:63], v[46:49], 0
	s_waitcnt lgkmcnt(2)
	v_mfma_f32_16x16x32_bf16 v[26:29], v[64:67], v[50:53], v[26:29]
	v_mfma_f32_16x16x32_bf16 v[60:63], v[64:67], v[54:57], v[60:63]
	s_nop 6
	v_cvt_pk_bf16_f32 v64, v26, v27
	v_cvt_pk_bf16_f32 v65, v28, v29
	v_cvt_pk_bf16_f32 v60, v60, v61
	v_cvt_pk_bf16_f32 v61, v62, v63
	ds_write_b64 v32, v[64:65]
	ds_write_b64 v36, v[60:61]
	ds_write_b16 v30, v60
	ds_write_b16_d16_hi v30, v60 offset:144
	ds_write_b16 v30, v61 offset:288
	ds_write_b16_d16_hi v30, v61 offset:432
	s_waitcnt lgkmcnt(6)
	v_mfma_f32_16x16x32_bf16 v[36:39], v[154:157], v[42:45], v[38:41]
	v_mfma_f32_16x16x32_bf16 v[40:43], v[154:157], v[46:49], 0
	v_mfma_f32_16x16x32_bf16 v[36:39], v[158:161], v[50:53], v[36:39]
	v_mfma_f32_16x16x32_bf16 v[40:43], v[158:161], v[54:57], v[40:43]
	s_nop 6
	v_cvt_pk_bf16_f32 v44, v36, v37
	v_cvt_pk_bf16_f32 v45, v38, v39
	ds_write_b64 v33, v[44:45]
	v_cvt_pk_bf16_f32 v40, v40, v41
	v_cvt_pk_bf16_f32 v41, v42, v43
	ds_write_b64 v72, v[40:41]
	ds_write_b16 v31, v40
	ds_write_b16_d16_hi v31, v40 offset:144
	ds_write_b16 v31, v41 offset:288
	ds_write_b16_d16_hi v31, v41 offset:432
	s_waitcnt lgkmcnt(0)
	s_barrier
	ds_read_b128 v[40:43], v35
	ds_read_b128 v[44:47], v74
	ds_read_b128 v[48:51], v35 offset:64
	ds_read_b128 v[52:55], v74 offset:64
	ds_read_b128 v[60:63], v59
	ds_read_b128 v[64:67], v59 offset:64
	ds_read_b128 v[154:157], v78
	ds_read_b128 v[158:161], v78 offset:64
	s_waitcnt lgkmcnt(3)
	v_mfma_f32_16x16x32_bf16 v[26:29], v[60:63], v[40:43], v[26:29]
	v_mfma_f32_16x16x32_bf16 v[60:63], v[60:63], v[44:47], 0
	s_waitcnt lgkmcnt(2)
	v_mfma_f32_16x16x32_bf16 v[26:29], v[64:67], v[48:51], v[26:29]
	v_mfma_f32_16x16x32_bf16 v[60:63], v[64:67], v[52:55], v[60:63]
	s_nop 6
	v_cvt_pk_bf16_f32 v56, v26, v27
	v_cvt_pk_bf16_f32 v57, v28, v29
	ds_write_b64 v34, v[56:57]
	v_cvt_pk_bf16_f32 v56, v60, v61
	v_cvt_pk_bf16_f32 v57, v62, v63
	ds_write_b64 v68, v[56:57] offset:27648
	ds_write_b16 v69, v56 offset:46080
	ds_write_b16_d16_hi v69, v56 offset:46224
	ds_write_b16 v69, v57 offset:46368
	ds_write_b16_d16_hi v69, v57 offset:46512
	s_waitcnt lgkmcnt(6)
	v_mfma_f32_16x16x32_bf16 v[36:39], v[154:157], v[40:43], v[36:39]
	v_mfma_f32_16x16x32_bf16 v[40:43], v[154:157], v[44:47], 0
	v_mfma_f32_16x16x32_bf16 v[36:39], v[158:161], v[48:51], v[36:39]
	v_mfma_f32_16x16x32_bf16 v[40:43], v[158:161], v[52:55], v[40:43]
	s_nop 6
	v_cvt_pk_bf16_f32 v44, v36, v37
	v_cvt_pk_bf16_f32 v45, v38, v39
	ds_write_b64 v73, v[44:45]
	v_cvt_pk_bf16_f32 v40, v40, v41
	v_cvt_pk_bf16_f32 v41, v42, v43
	ds_write_b64 v70, v[40:41] offset:27648
	ds_write_b16 v71, v40 offset:46080
	ds_write_b16_d16_hi v71, v40 offset:46224
	ds_write_b16 v71, v41 offset:46368
	ds_write_b16_d16_hi v71, v41 offset:46512
	s_waitcnt lgkmcnt(0)
	s_barrier
	ds_read_b128 v[40:43], v75
	ds_read_b128 v[44:47], v58 offset:46080
	s_waitcnt lgkmcnt(0)
	v_mfma_f32_16x16x32_bf16 v[26:29], v[44:47], v[40:43], v[26:29]
	ds_read_b128 v[44:47], v75 offset:64
	ds_read_b128 v[48:51], v58 offset:46144
	s_waitcnt lgkmcnt(0)
	v_mfma_f32_16x16x32_bf16 v[26:29], v[48:51], v[44:47], v[26:29]
	s_nop 7
	v_cvt_pk_bf16_f32 v26, v26, v27
	v_cvt_pk_bf16_f32 v27, v28, v29
	ds_write_b64 v32, v[26:27]
	ds_read_b128 v[26:29], v82 offset:46080
	s_waitcnt lgkmcnt(0)
	v_mfma_f32_16x16x32_bf16 v[26:29], v[26:29], v[40:43], v[36:39]
	s_nop 2
	ds_read_b128 v[36:39], v82 offset:46144
	s_waitcnt lgkmcnt(0)
	v_mfma_f32_16x16x32_bf16 v[26:29], v[36:39], v[44:47], v[26:29]
	s_nop 7
	v_cvt_pk_bf16_f32 v26, v26, v27
	v_cvt_pk_bf16_f32 v27, v28, v29
	ds_write_b64 v33, v[26:27]
	s_waitcnt lgkmcnt(0)
	s_barrier
	ds_read_b128 v[26:29], v35
	ds_read_b128 v[32:35], v35 offset:64
	ds_read_b128 v[36:39], v58 offset:9216
	ds_read_b128 v[44:47], v58 offset:9280
	s_waitcnt lgkmcnt(1)
	v_mfma_f32_16x16x32_bf16 v[36:39], v[36:39], v[26:29], 0
	ds_read_b128 v[40:43], v58
	s_waitcnt lgkmcnt(1)
	v_mfma_f32_16x16x32_bf16 v[36:39], v[44:47], v[32:35], v[36:39]
	ds_read_b128 v[44:47], v58 offset:64
	s_waitcnt lgkmcnt(1)
	v_mfma_f32_16x16x32_bf16 v[40:43], v[40:43], v[26:29], 0
	s_nop 4
	v_cvt_pk_bf16_f32 v36, v36, v37
	v_cvt_pk_bf16_f32 v37, v38, v39
	v_add_u32_e32 v38, v128, v144
	s_waitcnt lgkmcnt(0)
	v_mfma_f32_16x16x32_bf16 v[40:43], v[44:47], v[32:35], v[40:43]
	ds_write_b16 v38, v36
	ds_write_b16_d16_hi v38, v36 offset:144
	ds_write_b16 v38, v37 offset:288
	ds_write_b16_d16_hi v38, v37 offset:432
	s_nop 3
	v_cvt_pk_bf16_f32 v36, v40, v41
	v_cvt_pk_bf16_f32 v37, v42, v43
	ds_write_b16 v30, v36
	ds_write_b16_d16_hi v30, v36 offset:144
	ds_write_b16 v30, v37 offset:288
	ds_write_b16_d16_hi v30, v37 offset:432
	ds_read_b128 v[36:39], v82 offset:9216
	ds_read_b128 v[40:43], v82
	s_waitcnt lgkmcnt(1)
	v_mfma_f32_16x16x32_bf16 v[36:39], v[36:39], v[26:29], 0
	s_waitcnt lgkmcnt(0)
	v_mfma_f32_16x16x32_bf16 v[26:29], v[40:43], v[26:29], 0
	ds_read_b128 v[40:43], v82 offset:9280
	s_waitcnt lgkmcnt(0)
	v_mfma_f32_16x16x32_bf16 v[36:39], v[40:43], v[32:35], v[36:39]
	ds_read_b128 v[40:43], v82 offset:64
	s_nop 6
	v_cvt_pk_bf16_f32 v30, v36, v37
	s_waitcnt lgkmcnt(0)
	v_mfma_f32_16x16x32_bf16 v[26:29], v[40:43], v[32:35], v[26:29]
	v_add_u32_e32 v33, v128, v147
	v_cvt_pk_bf16_f32 v32, v38, v39
	ds_write_b16 v33, v30
	ds_write_b16_d16_hi v33, v30 offset:144
	ds_write_b16 v33, v32 offset:288
	ds_write_b16_d16_hi v33, v32 offset:432
	s_nop 1
	v_cvt_pk_bf16_f32 v26, v26, v27
	v_cvt_pk_bf16_f32 v27, v28, v29
	ds_write_b16 v31, v26
	ds_write_b16_d16_hi v31, v26 offset:144
	ds_write_b16 v31, v27 offset:288
	ds_write_b16_d16_hi v31, v27 offset:432
	v_add_u32_e32 v26, v117, v110
	v_add_u32_e32 v27, v119, v110
	s_waitcnt lgkmcnt(0)
	s_barrier
	ds_read_b128 v[54:57], v26
	ds_read_b128 v[50:53], v27
	ds_read_b128 v[46:49], v150 offset:36864
	ds_read_b128 v[42:45], v150 offset:55296
	ds_read_b128 v[38:41], v26 offset:64
	ds_read_b128 v[34:37], v27 offset:64
	ds_read_b128 v[30:33], v150 offset:36928
	ds_read_b128 v[26:29], v150 offset:55360
	ds_read_b32 v60, v129
	s_waitcnt lgkmcnt(0)
	v_mul_f32_e32 v60, 0x3fb8aa3b, v60
	v_exp_f32_e32 v104, v60
	ds_read_b128 v[60:63], v76
	ds_read_b128 v[64:67], v59
	ds_read_b128 v[68:71], v58 offset:64512
	s_waitcnt lgkmcnt(2)
	v_mfma_f32_16x16x32_bf16 v[72:75], v[60:63], v[54:57], 0
	ds_read_b128 v[154:157], v76 offset:64
	ds_read_b128 v[158:161], v59 offset:64
	ds_read_b128 v[162:165], v58 offset:64576
	v_mfma_f32_16x16x32_bf16 v[60:63], v[60:63], v[46:49], 0
	s_waitcnt lgkmcnt(2)
	v_mfma_f32_16x16x32_bf16 v[58:61], v[154:157], v[30:33], v[60:63]
	v_mfma_f32_16x16x32_bf16 v[72:75], v[154:157], v[38:41], v[72:75]
	s_nop 4
	ds_read_b64 v[62:63], v151 offset:18432
	s_nop 0
	v_pk_add_f32 v[58:59], v[94:95], v[58:59]
	v_pk_add_f32 v[60:61], v[96:97], v[60:61]
	v_pk_mul_f32 v[58:59], v[104:105], v[58:59] op_sel_hi:[0,1]
	v_pk_mul_f32 v[60:61], v[104:105], v[60:61] op_sel_hi:[0,1]
	s_waitcnt lgkmcnt(0)
	v_and_b32_e32 v77, 0xffff0000, v62
	v_lshlrev_b32_e32 v76, 16, v62
	v_pk_add_f32 v[76:77], v[72:73], v[76:77]
	v_and_b32_e32 v73, 0xffff0000, v63
	v_lshlrev_b32_e32 v72, 16, v63
	v_pk_add_f32 v[80:81], v[74:75], v[72:73]
	v_mfma_f32_16x16x32_bf16 v[72:75], v[64:67], v[54:57], 0
	v_cvt_pk_bf16_f32 v58, v58, v59
	v_cvt_pk_bf16_f32 v59, v60, v61
	v_mfma_f32_16x16x32_bf16 v[62:65], v[64:67], v[46:49], 0
	v_mfma_f32_16x16x32_bf16 v[62:65], v[68:71], v[42:45], v[62:65]
	v_mfma_f32_16x16x32_bf16 v[72:75], v[68:71], v[50:53], v[72:75]
	v_or_b32_e32 v70, v106, v92
	v_mov_b32_e32 v71, v107
	v_lshlrev_b64 v[70:71], 1, v[70:71]
	v_mfma_f32_16x16x32_bf16 v[62:65], v[158:161], v[30:33], v[62:65]
	v_lshl_add_u64 v[60:61], s[78:79], 0, v[70:71]
	global_store_dwordx2 v[60:61], v[58:59], off
	v_lshl_add_u64 v[60:61], s[76:77], 0, v[70:71]
	v_mfma_f32_16x16x32_bf16 v[66:69], v[158:161], v[38:41], v[72:75]
	v_or_b32_e32 v106, v106, v98
	v_mfma_f32_16x16x32_bf16 v[62:65], v[162:165], v[26:29], v[62:65]
	s_nop 0
	v_cvt_pk_bf16_f32 v72, v76, v77
	v_cvt_pk_bf16_f32 v73, v80, v81
	v_lshl_add_u64 v[74:75], s[80:81], 0, v[70:71]
	v_mfma_f32_16x16x32_bf16 v[66:69], v[162:165], v[34:37], v[66:69]
	global_store_dwordx2 v[74:75], v[72:73], off
	s_nop 1
	v_pk_mul_f32 v[62:63], v[104:105], v[62:63] op_sel_hi:[0,1]
	v_pk_mul_f32 v[64:65], v[104:105], v[64:65] op_sel_hi:[0,1]
	v_cvt_pk_bf16_f32 v58, v62, v63
	v_cvt_pk_bf16_f32 v59, v64, v65
	s_nop 0
	v_cvt_pk_bf16_f32 v66, v66, v67
	v_cvt_pk_bf16_f32 v67, v68, v69
	v_lshl_add_u64 v[68:69], s[94:95], 0, v[70:71]
	global_store_dwordx2 v[68:69], v[66:67], off
	global_store_dwordx2 v[60:61], v[58:59], off
	v_add_u32_e32 v70, v130, v145
	ds_read_b128 v[66:69], v70
	ds_read_b128 v[62:65], v78
	ds_read_b128 v[58:61], v82 offset:64512
	s_waitcnt lgkmcnt(2)
	v_mfma_f32_16x16x32_bf16 v[74:77], v[66:69], v[54:57], 0
	ds_read_b128 v[70:73], v70 offset:64
	ds_read_b128 v[78:81], v78 offset:64
	ds_read_b128 v[82:85], v82 offset:64576
	s_waitcnt lgkmcnt(4)
	v_mfma_f32_16x16x32_bf16 v[54:57], v[62:65], v[54:57], 0
	v_mfma_f32_16x16x32_bf16 v[66:69], v[66:69], v[46:49], 0
	v_mfma_f32_16x16x32_bf16 v[46:49], v[62:65], v[46:49], 0
	s_waitcnt lgkmcnt(3)
	v_mfma_f32_16x16x32_bf16 v[50:53], v[58:61], v[50:53], v[54:57]
	v_mfma_f32_16x16x32_bf16 v[42:45], v[58:61], v[42:45], v[46:49]
	s_waitcnt lgkmcnt(2)
	v_mfma_f32_16x16x32_bf16 v[74:77], v[70:73], v[38:41], v[74:77]
	v_mfma_f32_16x16x32_bf16 v[66:69], v[70:73], v[30:33], v[66:69]
	ds_read_b64 v[70:71], v152 offset:18432
	s_waitcnt lgkmcnt(0)
	v_and_b32_e32 v73, 0xffff0000, v70
	v_mfma_f32_16x16x32_bf16 v[38:41], v[78:81], v[38:41], v[50:53]
	v_lshlrev_b32_e32 v72, 16, v70
	s_nop 1
	v_pk_add_f32 v[72:73], v[74:75], v[72:73]
	v_and_b32_e32 v75, 0xffff0000, v71
	v_mfma_f32_16x16x32_bf16 v[30:33], v[78:81], v[30:33], v[42:45]
	v_lshlrev_b32_e32 v74, 16, v71
	v_pk_add_f32 v[70:71], v[76:77], v[74:75]
	v_mfma_f32_16x16x32_bf16 v[34:37], v[82:85], v[34:37], v[38:41]
	v_mfma_f32_16x16x32_bf16 v[26:29], v[82:85], v[26:29], v[30:33]
	s_nop 3
	v_lshlrev_b64 v[32:33], 1, v[106:107]
	v_cvt_pk_bf16_f32 v30, v72, v73
	v_cvt_pk_bf16_f32 v31, v70, v71
	v_lshl_add_u64 v[38:39], s[80:81], 0, v[32:33]
	global_store_dwordx2 v[38:39], v[30:31], off
	v_cvt_pk_bf16_f32 v30, v34, v35
	v_cvt_pk_bf16_f32 v31, v36, v37
	v_lshl_add_u64 v[34:35], s[94:95], 0, v[32:33]
	global_store_dwordx2 v[34:35], v[30:31], off
	v_pk_add_f32 v[30:31], v[100:101], v[66:67]
	v_pk_mul_f32 v[26:27], v[104:105], v[26:27] op_sel_hi:[0,1]
	v_pk_add_f32 v[34:35], v[102:103], v[68:69]
	v_pk_mul_f32 v[28:29], v[104:105], v[28:29] op_sel_hi:[0,1]
	v_pk_mul_f32 v[30:31], v[104:105], v[30:31] op_sel_hi:[0,1]
	v_pk_mul_f32 v[34:35], v[104:105], v[34:35] op_sel_hi:[0,1]
	v_cvt_pk_bf16_f32 v26, v26, v27
	v_cvt_pk_bf16_f32 v27, v28, v29
	v_lshl_add_u64 v[28:29], s[76:77], 0, v[32:33]
	v_readlane_b32 s76, v252, 0
	v_cvt_pk_bf16_f32 v30, v30, v31
	v_cvt_pk_bf16_f32 v31, v34, v35
	v_lshl_add_u64 v[34:35], s[78:79], 0, v[32:33]
	s_add_i32 s90, s90, s76
	global_store_dwordx2 v[34:35], v[30:31], off
	global_store_dwordx2 v[28:29], v[26:27], off
	v_readlane_b32 s77, v252, 1
	s_cbranch_vccz .LBB0_1858

.LBB0_1835:
	s_or_b64 exec, exec, s[70:71]
	v_mov_b32_e32 v87, v86
	v_mov_b64_e32 v[58:59], v[86:87]
	v_mov_b64_e32 v[62:63], v[86:87]
	v_mov_b64_e32 v[60:61], v[86:87]
	v_mov_b64_e32 v[64:65], v[86:87]
	s_waitcnt lgkmcnt(0)
	s_barrier
	s_mov_b64 s[70:71], exec
	s_and_b64 exec, exec, s[12:13]
	s_cbranch_execz .Lr1p_rd
	ds_read_b128 v[166:169], v134
	ds_read_b128 v[170:173], v134 offset:16
	s_and_b64 exec, exec, s[14:15]
	s_cbranch_execz .Lr1p_rd
	ds_read_b128 v[174:177], v135
	ds_read_b128 v[178:181], v135 offset:16
	s_and_b64 exec, exec, s[16:17]
	s_cbranch_execz .Lr1p_rd
	ds_read_b128 v[182:185], v136
	ds_read_b128 v[186:189], v136 offset:16
	s_and_b64 exec, exec, s[18:19]
	s_cbranch_execz .Lr1p_rd
	ds_read_b128 v[190:193], v137
	ds_read_b128 v[194:197], v137 offset:16
	s_and_b64 exec, exec, s[20:21]
	s_cbranch_execz .Lr1p_rd
	ds_read_b128 v[198:201], v138
	ds_read_b128 v[202:205], v138 offset:16
	s_and_b64 exec, exec, s[22:23]
	s_cbranch_execz .Lr1p_rd
	ds_read_b128 v[206:209], v139
	ds_read_b128 v[210:213], v139 offset:16
	s_and_b64 exec, exec, s[24:25]
	s_cbranch_execz .Lr1p_rd
	ds_read_b128 v[214:217], v140
	ds_read_b128 v[218:221], v140 offset:16
	s_and_b64 exec, exec, s[26:27]
	s_cbranch_execz .Lr1p_rd
	ds_read_b128 v[222:225], v141
	ds_read_b128 v[226:229], v141 offset:16
.Lr1p_rd:
	s_mov_b64 exec, s[70:71]
	s_waitcnt lgkmcnt(0)
	s_and_b64 exec, exec, s[12:13]
	s_cbranch_execz .Lr1p_ad
	v_pk_add_f32 v[64:65], v[166:167], 0 op_sel_hi:[1,0]
	v_pk_add_f32 v[60:61], v[168:169], 0 op_sel_hi:[1,0]
	v_pk_add_f32 v[62:63], v[170:171], 0 op_sel_hi:[1,0]
	v_pk_add_f32 v[58:59], v[172:173], 0 op_sel_hi:[1,0]
	s_and_b64 exec, exec, s[14:15]
	s_cbranch_execz .Lr1p_ad
	v_pk_add_f32 v[64:65], v[64:65], v[174:175]
	v_pk_add_f32 v[60:61], v[60:61], v[176:177]
	v_pk_add_f32 v[62:63], v[62:63], v[178:179]
	v_pk_add_f32 v[58:59], v[58:59], v[180:181]
	s_and_b64 exec, exec, s[16:17]
	s_cbranch_execz .Lr1p_ad
	v_pk_add_f32 v[64:65], v[64:65], v[182:183]
	v_pk_add_f32 v[60:61], v[60:61], v[184:185]
	v_pk_add_f32 v[62:63], v[62:63], v[186:187]
	v_pk_add_f32 v[58:59], v[58:59], v[188:189]
	s_and_b64 exec, exec, s[18:19]
	s_cbranch_execz .Lr1p_ad
	v_pk_add_f32 v[64:65], v[64:65], v[190:191]
	v_pk_add_f32 v[60:61], v[60:61], v[192:193]
	v_pk_add_f32 v[62:63], v[62:63], v[194:195]
	v_pk_add_f32 v[58:59], v[58:59], v[196:197]
	s_and_b64 exec, exec, s[20:21]
	s_cbranch_execz .Lr1p_ad
	v_pk_add_f32 v[64:65], v[64:65], v[198:199]
	v_pk_add_f32 v[60:61], v[60:61], v[200:201]
	v_pk_add_f32 v[62:63], v[62:63], v[202:203]
	v_pk_add_f32 v[58:59], v[58:59], v[204:205]
	s_and_b64 exec, exec, s[22:23]
	s_cbranch_execz .Lr1p_ad
	v_pk_add_f32 v[64:65], v[64:65], v[206:207]
	v_pk_add_f32 v[60:61], v[60:61], v[208:209]
	v_pk_add_f32 v[62:63], v[62:63], v[210:211]
	v_pk_add_f32 v[58:59], v[58:59], v[212:213]
	s_and_b64 exec, exec, s[24:25]
	s_cbranch_execz .Lr1p_ad
	v_pk_add_f32 v[64:65], v[64:65], v[214:215]
	v_pk_add_f32 v[60:61], v[60:61], v[216:217]
	v_pk_add_f32 v[62:63], v[62:63], v[218:219]
	v_pk_add_f32 v[58:59], v[58:59], v[220:221]
	s_and_b64 exec, exec, s[26:27]
	s_cbranch_execz .Lr1p_ad
	v_pk_add_f32 v[64:65], v[64:65], v[222:223]
	v_pk_add_f32 v[60:61], v[60:61], v[224:225]
	v_pk_add_f32 v[62:63], v[62:63], v[226:227]
	v_pk_add_f32 v[58:59], v[58:59], v[228:229]
.Lr1p_ad:
	s_mov_b64 exec, s[70:71]
	v_cndmask_b32_e64 v39, v39, v51, s[10:11]
	v_cndmask_b32_e64 v38, v38, v50, s[10:11]
	v_cndmask_b32_e64 v41, v41, v53, s[10:11]
	v_cndmask_b32_e64 v40, v40, v52, s[10:11]
	v_cndmask_b32_e64 v35, v35, v55, s[10:11]
	v_cndmask_b32_e64 v34, v34, v54, s[10:11]
	v_cndmask_b32_e64 v37, v37, v57, s[10:11]
	v_cndmask_b32_e64 v36, v36, v56, s[10:11]
	v_pk_add_f32 v[38:39], v[38:39], v[64:65]
	v_pk_add_f32 v[40:41], v[40:41], v[60:61]
	v_pk_add_f32 v[34:35], v[34:35], v[62:63]
	v_pk_add_f32 v[36:37], v[36:37], v[58:59]
	s_and_saveexec_b64 s[70:71], s[4:5]
	s_cbranch_execz .LBB0_1846
	ds_write_b128 v105, v[38:41]
	ds_write_b128 v105, v[34:37] offset:16

.LBB0_1849:
	s_andn2_b64 vcc, exec, s[88:89]
	s_cbranch_vccnz .LBB0_1831
	v_mov_b32_e32 v2, v3
	s_branch .LBB0_1831
.LBB0_1858:
	v_readlane_b32 s48, v252, 3
	v_readlane_b32 s80, v252, 13
	v_readlane_b32 s82, v252, 9
	v_readlane_b32 s49, v252, 4
	v_readlane_b32 s50, v252, 5
	v_readlane_b32 s51, v252, 6
	v_readlane_b32 s81, v252, 14
	v_readlane_b32 s83, v252, 10
